# P9 epilogue: both SwiGLU rounds staged at once (round 1 slabs in the idle ring slots As[1][0..1]): 2 workgroup barriers and one LDS round trip per unit instead of 4 and 2
# speedup vs baseline: 1.0062x; 1.0062x over previous
; #define LAS __attribute__((address_space(3)))
; __device__ __forceinline__ unsigned pk4_fp8(float a, float b, float c, float d) { int w = 0; w = __builtin_amdgcn_cvt_pk_fp8_f32(a, b, w, false); w = __builtin_amdgcn_cvt_pk_fp8_f32(c, d, w, true); return (unsigned)w; }
;     __device__ __forceinline__ void operator()(const f32x4 (&acc)[2][2][4][2], const Unit& u, int wr, int wc, int fr, int fq) const {
;         const int e = u.pn / npn, pnl = u.pn - e * npn; const int tid = threadIdx.x;
;         const int col0 = pnl * BM + wc * 32 + 8 * fq;
;         f32x4 bv[2][2];
; #pragma unroll
;         for (int bj = 0; bj < 2; ++bj)
; #pragma unroll
;             for (int n = 0; n < 2; ++n) bv[bj][n] = *(const f32x4*)(bias + (size_t)e * bias_ld + col0 + bj * HALF + 4 * n);
;         LAS unsigned char* wp = stg + (16 * wr + fr) * STG8_PITCH + 16 * wc + 4 * fq;
;         const int rr = (tid >> 3) & 31, cc = tid & 7, ms = tid >> 8;
;         const LAS unsigned char* rp = stg + rr * STG8_PITCH + cc * 16;
;         unsigned char* gp = O + (size_t)(u.pm * BM + 64 * (rr >> 4) + (rr & 15)) * ldc + pnl * (BM / 2) + cc * 16;
; #pragma unroll
;         for (int ai = 0; ai < 2; ++ai) {
; #pragma unroll
;             for (int m = 0; m < 4; ++m)
; #pragma unroll
;                 for (int bj = 0; bj < 2; ++bj) { const f32x4 v0 = acc[ai][bj][m][0] * scale + bv[bj][0], v1 = acc[ai][bj][m][1] * scale + bv[bj][1];
;                     *(LAS unsigned*)(wp + m * (32 * STG8_PITCH) + 64 * bj) = pk4_fp8(swiglu1(v0[0], v0[1]), swiglu1(v0[2], v0[3]), swiglu1(v1[0], v1[1]), swiglu1(v1[2], v1[3])); }
.LBB0_1010:
	s_cmp_eq_u32 s42, s46
	s_cselect_b32 s55, s23, s19
	s_ashr_i32 s2, s23, 31
	s_lshr_b32 s2, s2, 28
	s_add_i32 s3, s23, s2
	s_and_b32 s3, s3, -16
	s_sub_i32 s23, s23, s3
	s_ashr_i32 s2, s55, 31
	s_lshr_b32 s2, s2, 28
	s_add_i32 s3, s55, s2
	s_ashr_i32 s2, s3, 4
	s_and_b32 s3, s3, -16
	s_sub_i32 s54, s55, s3
	s_ashr_i32 s3, s2, 31
	s_lshl_b64 s[2:3], s[2:3], 14
	v_readlane_b32 s52, v254, 0
	v_lshl_or_b32 v2, s54, 8, v200
	v_readlane_b32 s53, v254, 1
	s_add_u32 s2, s52, s2
	s_addc_u32 s3, s53, s3
	v_ashrrev_i32_e32 v3, 31, v2
	s_nop 15
	s_nop 15
	v_lshl_add_u64 v[2:3], v[2:3], 2, s[2:3]
	global_load_dwordx4 v[208:211], v[2:3], off
	global_load_dwordx4 v[212:215], v[2:3], off offset:16
	global_load_dwordx4 v[216:219], v[2:3], off offset:512
	global_load_dwordx4 v[220:223], v[2:3], off offset:528
	v_lshl_or_b32 v18, s22, 8, v201
	v_ashrrev_i32_e32 v19, 31, v18
	v_lshlrev_b64 v[18:19], 11, v[18:19]
	s_lshl_b32 s22, s23, 7
	v_lshl_add_u64 v[18:19], s[8:9], 0, v[18:19]
	s_ashr_i32 s23, s22, 31
	v_lshl_add_u64 v[18:19], v[18:19], 0, s[22:23]
	v_lshl_add_u64 v[18:19], v[18:19], 0, v[170:171]
	s_cmp_eq_u32 s42, s46
	s_mov_b64 s[2:3], -1
	v_readlane_b32 s54, v254, 2
	v_readlane_b32 s55, v254, 3
	v_readlane_b32 s56, v254, 4
	v_readlane_b32 s57, v254, 5
	v_readlane_b32 s58, v254, 6
	v_readlane_b32 s59, v254, 7
	v_add_u32_e32 v22, 0x1000, v202
	v_add_u32_e32 v23, 0x2400, v202
	v_add_u32_e32 v24, 0x3400, v202
	v_min_f32_e32 v158, 0x43e00000, v158
	v_min_f32_e32 v160, 0x43e00000, v160
	v_min_f32_e32 v154, 0x43e00000, v154
	v_min_f32_e32 v156, 0x43e00000, v156
	v_mul_f32_e32 v2, 0xbd1d265f, v158
	v_mul_f32_e32 v3, 0xbd1d265f, v160
	v_mul_f32_e32 v4, 0xbd1d265f, v154
	v_mul_f32_e32 v5, 0xbd1d265f, v156
	v_exp_f32_e32 v2, v2
	v_exp_f32_e32 v3, v3
	v_exp_f32_e32 v4, v4
	v_exp_f32_e32 v5, v5
	v_fma_f32 v2, v2, v246, v246
	v_fma_f32 v3, v3, v246, v246
	v_fma_f32 v4, v4, v246, v246
	v_fma_f32 v5, v5, v246, v246
	v_rcp_f32_e32 v2, v2
	v_rcp_f32_e32 v3, v3
	v_rcp_f32_e32 v4, v4
	v_rcp_f32_e32 v5, v5
	v_med3_f32 v159, v159, s47, v204
	v_med3_f32 v161, v161, s47, v204
	v_med3_f32 v155, v155, s47, v204
	v_med3_f32 v157, v157, s47, v204
	v_mul_f32_e32 v158, v158, v2
	v_mul_f32_e32 v160, v160, v3
	v_mul_f32_e32 v154, v154, v4
	v_mul_f32_e32 v156, v156, v5
	v_mul_f32_e32 v158, v158, v159
	v_mul_f32_e32 v160, v160, v161
	v_mul_f32_e32 v154, v154, v155
	v_mul_f32_e32 v156, v156, v157
	v_cvt_pk_fp8_f32 v6, v158, v160
	v_cvt_pk_fp8_f32 v6, v154, v156 op_sel:[0,0,1]
	v_min_f32_e32 v150, 0x43e00000, v150
	v_min_f32_e32 v152, 0x43e00000, v152
	v_min_f32_e32 v146, 0x43e00000, v146
	v_min_f32_e32 v148, 0x43e00000, v148
	v_mul_f32_e32 v2, 0xbd1d265f, v150
	v_mul_f32_e32 v3, 0xbd1d265f, v152
	v_mul_f32_e32 v4, 0xbd1d265f, v146
	v_mul_f32_e32 v5, 0xbd1d265f, v148
	v_exp_f32_e32 v2, v2
	v_exp_f32_e32 v3, v3
	v_exp_f32_e32 v4, v4
	v_exp_f32_e32 v5, v5
	v_fma_f32 v2, v2, v246, v246
	v_fma_f32 v3, v3, v246, v246
	v_fma_f32 v4, v4, v246, v246
	v_fma_f32 v5, v5, v246, v246
	v_rcp_f32_e32 v2, v2
	v_rcp_f32_e32 v3, v3
	v_rcp_f32_e32 v4, v4
	v_rcp_f32_e32 v5, v5
	v_med3_f32 v151, v151, s47, v204
	v_med3_f32 v153, v153, s47, v204
	v_med3_f32 v147, v147, s47, v204
	v_med3_f32 v149, v149, s47, v204
	v_mul_f32_e32 v150, v150, v2
	v_mul_f32_e32 v152, v152, v3
	v_mul_f32_e32 v146, v146, v4
	v_mul_f32_e32 v148, v148, v5
	v_mul_f32_e32 v150, v150, v151
	v_mul_f32_e32 v152, v152, v153
	v_mul_f32_e32 v146, v146, v147
	v_mul_f32_e32 v148, v148, v149
	v_cvt_pk_fp8_f32 v7, v150, v152
	v_cvt_pk_fp8_f32 v7, v146, v148 op_sel:[0,0,1]
	v_min_f32_e32 v142, 0x43e00000, v142
	v_min_f32_e32 v144, 0x43e00000, v144
	v_min_f32_e32 v138, 0x43e00000, v138
	v_min_f32_e32 v140, 0x43e00000, v140
	v_mul_f32_e32 v2, 0xbd1d265f, v142
	v_mul_f32_e32 v3, 0xbd1d265f, v144
	v_mul_f32_e32 v4, 0xbd1d265f, v138
	v_mul_f32_e32 v5, 0xbd1d265f, v140
	v_exp_f32_e32 v2, v2
	v_exp_f32_e32 v3, v3
	v_exp_f32_e32 v4, v4
	v_exp_f32_e32 v5, v5
	v_fma_f32 v2, v2, v246, v246
	v_fma_f32 v3, v3, v246, v246
	v_fma_f32 v4, v4, v246, v246
	v_fma_f32 v5, v5, v246, v246
	v_rcp_f32_e32 v2, v2
	v_rcp_f32_e32 v3, v3
	v_rcp_f32_e32 v4, v4
	v_rcp_f32_e32 v5, v5
	v_med3_f32 v143, v143, s47, v204
	v_med3_f32 v145, v145, s47, v204
	v_med3_f32 v139, v139, s47, v204
	v_med3_f32 v141, v141, s47, v204
	v_mul_f32_e32 v142, v142, v2
	v_mul_f32_e32 v144, v144, v3
	v_mul_f32_e32 v138, v138, v4
	v_mul_f32_e32 v140, v140, v5
	v_mul_f32_e32 v142, v142, v143
	v_mul_f32_e32 v144, v144, v145
	v_mul_f32_e32 v138, v138, v139
	v_mul_f32_e32 v140, v140, v141
	v_cvt_pk_fp8_f32 v8, v142, v144
	v_cvt_pk_fp8_f32 v8, v138, v140 op_sel:[0,0,1]
	v_min_f32_e32 v134, 0x43e00000, v134
	v_min_f32_e32 v136, 0x43e00000, v136
	v_min_f32_e32 v130, 0x43e00000, v130
	v_min_f32_e32 v132, 0x43e00000, v132
	v_mul_f32_e32 v2, 0xbd1d265f, v134
	v_mul_f32_e32 v3, 0xbd1d265f, v136
	v_mul_f32_e32 v4, 0xbd1d265f, v130
	v_mul_f32_e32 v5, 0xbd1d265f, v132
	v_exp_f32_e32 v2, v2
	v_exp_f32_e32 v3, v3
	v_exp_f32_e32 v4, v4
	v_exp_f32_e32 v5, v5
	v_fma_f32 v2, v2, v246, v246
	v_fma_f32 v3, v3, v246, v246
	v_fma_f32 v4, v4, v246, v246
	v_fma_f32 v5, v5, v246, v246
	v_rcp_f32_e32 v2, v2
	v_rcp_f32_e32 v3, v3
	v_rcp_f32_e32 v4, v4
	v_rcp_f32_e32 v5, v5
	v_med3_f32 v135, v135, s47, v204
	v_med3_f32 v137, v137, s47, v204
	v_med3_f32 v131, v131, s47, v204
	v_med3_f32 v133, v133, s47, v204
	v_mul_f32_e32 v134, v134, v2
	v_mul_f32_e32 v136, v136, v3
	v_mul_f32_e32 v130, v130, v4
	v_mul_f32_e32 v132, v132, v5
	v_mul_f32_e32 v134, v134, v135
	v_mul_f32_e32 v136, v136, v137
	v_mul_f32_e32 v130, v130, v131
	v_mul_f32_e32 v132, v132, v133
	v_cvt_pk_fp8_f32 v9, v134, v136
	v_cvt_pk_fp8_f32 v9, v130, v132 op_sel:[0,0,1]
; #define LAS __attribute__((address_space(3)))
; __device__ __forceinline__ unsigned pk4_fp8(float a, float b, float c, float d) { int w = 0; w = __builtin_amdgcn_cvt_pk_fp8_f32(a, b, w, false); w = __builtin_amdgcn_cvt_pk_fp8_f32(c, d, w, true); return (unsigned)w; }
;     __device__ __forceinline__ void operator()(const f32x4 (&acc)[2][2][4][2], const Unit& u, int wr, int wc, int fr, int fq) const {
;     ...
;         for (int ai = 0; ai < 2; ++ai) {
; #pragma unroll
;             for (int m = 0; m < 4; ++m)
; #pragma unroll
;                 for (int bj = 0; bj < 2; ++bj) { const f32x4 v0 = acc[ai][bj][m][0] * scale + bv[bj][0], v1 = acc[ai][bj][m][1] * scale + bv[bj][1];
;                     *(LAS unsigned*)(wp + m * (32 * STG8_PITCH) + 64 * bj) = pk4_fp8(swiglu1(v0[0], v0[1]), swiglu1(v0[2], v0[3]), swiglu1(v1[0], v1[1]), swiglu1(v1[2], v1[3])); }
;             asm volatile("s_waitcnt lgkmcnt(0)" ::: "memory"); __builtin_amdgcn_s_barrier(); asm volatile("" ::: "memory");
; #pragma unroll
;             for (int k2 = 0; k2 < 2; ++k2) { const int m = ms + 2 * k2;
;                 *(u32x4*)(gp + (size_t)(ai * HALF + m * 16) * ldc) = *(const LAS u32x4*)(rp + m * (32 * STG8_PITCH)); }
;             asm volatile("s_waitcnt lgkmcnt(0)" ::: "memory"); __builtin_amdgcn_s_barrier(); asm volatile("" ::: "memory");
;         }
	v_min_f32_e32 v126, 0x43e00000, v126
	v_min_f32_e32 v128, 0x43e00000, v128
	v_min_f32_e32 v122, 0x43e00000, v122
	v_min_f32_e32 v124, 0x43e00000, v124
	v_mul_f32_e32 v2, 0xbd1d265f, v126
	v_mul_f32_e32 v3, 0xbd1d265f, v128
	v_mul_f32_e32 v4, 0xbd1d265f, v122
	v_mul_f32_e32 v5, 0xbd1d265f, v124
	v_exp_f32_e32 v2, v2
	v_exp_f32_e32 v3, v3
	v_exp_f32_e32 v4, v4
	v_exp_f32_e32 v5, v5
	v_fma_f32 v2, v2, v246, v246
	v_fma_f32 v3, v3, v246, v246
	v_fma_f32 v4, v4, v246, v246
	v_fma_f32 v5, v5, v246, v246
	v_rcp_f32_e32 v2, v2
	v_rcp_f32_e32 v3, v3
	v_rcp_f32_e32 v4, v4
	v_rcp_f32_e32 v5, v5
	v_med3_f32 v127, v127, s47, v204
	v_med3_f32 v129, v129, s47, v204
	v_med3_f32 v123, v123, s47, v204
	v_med3_f32 v125, v125, s47, v204
	v_mul_f32_e32 v126, v126, v2
	v_mul_f32_e32 v128, v128, v3
	v_mul_f32_e32 v122, v122, v4
	v_mul_f32_e32 v124, v124, v5
	v_mul_f32_e32 v126, v126, v127
	v_mul_f32_e32 v128, v128, v129
	v_mul_f32_e32 v122, v122, v123
	v_mul_f32_e32 v124, v124, v125
	v_cvt_pk_fp8_f32 v10, v126, v128
	v_cvt_pk_fp8_f32 v10, v122, v124 op_sel:[0,0,1]
	v_min_f32_e32 v118, 0x43e00000, v118
	v_min_f32_e32 v120, 0x43e00000, v120
	v_min_f32_e32 v114, 0x43e00000, v114
	v_min_f32_e32 v116, 0x43e00000, v116
	v_mul_f32_e32 v2, 0xbd1d265f, v118
	v_mul_f32_e32 v3, 0xbd1d265f, v120
	v_mul_f32_e32 v4, 0xbd1d265f, v114
	v_mul_f32_e32 v5, 0xbd1d265f, v116
	v_exp_f32_e32 v2, v2
	v_exp_f32_e32 v3, v3
	v_exp_f32_e32 v4, v4
	v_exp_f32_e32 v5, v5
	v_fma_f32 v2, v2, v246, v246
	v_fma_f32 v3, v3, v246, v246
	v_fma_f32 v4, v4, v246, v246
	v_fma_f32 v5, v5, v246, v246
	v_rcp_f32_e32 v2, v2
	v_rcp_f32_e32 v3, v3
	v_rcp_f32_e32 v4, v4
	v_rcp_f32_e32 v5, v5
	v_med3_f32 v119, v119, s47, v204
	v_med3_f32 v121, v121, s47, v204
	v_med3_f32 v115, v115, s47, v204
	v_med3_f32 v117, v117, s47, v204
	v_mul_f32_e32 v118, v118, v2
	v_mul_f32_e32 v120, v120, v3
	v_mul_f32_e32 v114, v114, v4
	v_mul_f32_e32 v116, v116, v5
	v_mul_f32_e32 v118, v118, v119
	v_mul_f32_e32 v120, v120, v121
	v_mul_f32_e32 v114, v114, v115
	v_mul_f32_e32 v116, v116, v117
	v_cvt_pk_fp8_f32 v11, v118, v120
	v_cvt_pk_fp8_f32 v11, v114, v116 op_sel:[0,0,1]
	v_min_f32_e32 v110, 0x43e00000, v110
	v_min_f32_e32 v112, 0x43e00000, v112
	v_min_f32_e32 v106, 0x43e00000, v106
	v_min_f32_e32 v108, 0x43e00000, v108
	v_mul_f32_e32 v2, 0xbd1d265f, v110
	v_mul_f32_e32 v3, 0xbd1d265f, v112
	v_mul_f32_e32 v4, 0xbd1d265f, v106
	v_mul_f32_e32 v5, 0xbd1d265f, v108
	v_exp_f32_e32 v2, v2
	v_exp_f32_e32 v3, v3
	v_exp_f32_e32 v4, v4
	v_exp_f32_e32 v5, v5
	v_fma_f32 v2, v2, v246, v246
	v_fma_f32 v3, v3, v246, v246
	v_fma_f32 v4, v4, v246, v246
	v_fma_f32 v5, v5, v246, v246
	v_rcp_f32_e32 v2, v2
	v_rcp_f32_e32 v3, v3
	v_rcp_f32_e32 v4, v4
	v_rcp_f32_e32 v5, v5
	v_med3_f32 v111, v111, s47, v204
	v_med3_f32 v113, v113, s47, v204
	v_med3_f32 v107, v107, s47, v204
	v_med3_f32 v109, v109, s47, v204
	v_mul_f32_e32 v110, v110, v2
	v_mul_f32_e32 v112, v112, v3
	v_mul_f32_e32 v106, v106, v4
	v_mul_f32_e32 v108, v108, v5
	v_mul_f32_e32 v110, v110, v111
	v_mul_f32_e32 v112, v112, v113
	v_mul_f32_e32 v106, v106, v107
	v_mul_f32_e32 v108, v108, v109
	v_cvt_pk_fp8_f32 v12, v110, v112
	v_cvt_pk_fp8_f32 v12, v106, v108 op_sel:[0,0,1]
	v_min_f32_e32 v102, 0x43e00000, v102
	v_min_f32_e32 v104, 0x43e00000, v104
	v_min_f32_e32 v98, 0x43e00000, v98
	v_min_f32_e32 v100, 0x43e00000, v100
	v_mul_f32_e32 v2, 0xbd1d265f, v102
	v_mul_f32_e32 v3, 0xbd1d265f, v104
	v_mul_f32_e32 v4, 0xbd1d265f, v98
	v_mul_f32_e32 v5, 0xbd1d265f, v100
	v_exp_f32_e32 v2, v2
	v_exp_f32_e32 v3, v3
	v_exp_f32_e32 v4, v4
	v_exp_f32_e32 v5, v5
	v_fma_f32 v2, v2, v246, v246
	v_fma_f32 v3, v3, v246, v246
	v_fma_f32 v4, v4, v246, v246
	v_fma_f32 v5, v5, v246, v246
	v_rcp_f32_e32 v2, v2
	v_rcp_f32_e32 v3, v3
	v_rcp_f32_e32 v4, v4
	v_rcp_f32_e32 v5, v5
	v_med3_f32 v103, v103, s47, v204
	v_med3_f32 v105, v105, s47, v204
	v_med3_f32 v99, v99, s47, v204
	v_med3_f32 v101, v101, s47, v204
	v_mul_f32_e32 v102, v102, v2
	v_mul_f32_e32 v104, v104, v3
	v_mul_f32_e32 v98, v98, v4
	v_mul_f32_e32 v100, v100, v5
	v_mul_f32_e32 v102, v102, v103
	v_mul_f32_e32 v104, v104, v105
	v_mul_f32_e32 v98, v98, v99
	v_mul_f32_e32 v100, v100, v101
	v_cvt_pk_fp8_f32 v13, v102, v104
	v_cvt_pk_fp8_f32 v13, v98, v100 op_sel:[0,0,1]
	v_min_f32_e32 v94, 0x43e00000, v94
	v_min_f32_e32 v96, 0x43e00000, v96
	v_min_f32_e32 v90, 0x43e00000, v90
	v_min_f32_e32 v92, 0x43e00000, v92
	v_mul_f32_e32 v2, 0xbd1d265f, v94
	v_mul_f32_e32 v3, 0xbd1d265f, v96
	v_mul_f32_e32 v4, 0xbd1d265f, v90
	v_mul_f32_e32 v5, 0xbd1d265f, v92
	v_exp_f32_e32 v2, v2
	v_exp_f32_e32 v3, v3
	v_exp_f32_e32 v4, v4
	v_exp_f32_e32 v5, v5
	v_fma_f32 v2, v2, v246, v246
	v_fma_f32 v3, v3, v246, v246
	v_fma_f32 v4, v4, v246, v246
	v_fma_f32 v5, v5, v246, v246
	v_rcp_f32_e32 v2, v2
	v_rcp_f32_e32 v3, v3
	v_rcp_f32_e32 v4, v4
	v_rcp_f32_e32 v5, v5
	v_med3_f32 v95, v95, s47, v204
	v_med3_f32 v97, v97, s47, v204
	v_med3_f32 v91, v91, s47, v204
	v_med3_f32 v93, v93, s47, v204
	v_mul_f32_e32 v94, v94, v2
	v_mul_f32_e32 v96, v96, v3
	v_mul_f32_e32 v90, v90, v4
	v_mul_f32_e32 v92, v92, v5
	v_mul_f32_e32 v94, v94, v95
	v_mul_f32_e32 v96, v96, v97
	v_mul_f32_e32 v90, v90, v91
	v_mul_f32_e32 v92, v92, v93
	v_cvt_pk_fp8_f32 v26, v94, v96
	v_cvt_pk_fp8_f32 v26, v90, v92 op_sel:[0,0,1]
	v_min_f32_e32 v86, 0x43e00000, v86
	v_min_f32_e32 v88, 0x43e00000, v88
	v_min_f32_e32 v82, 0x43e00000, v82
	v_min_f32_e32 v84, 0x43e00000, v84
	v_mul_f32_e32 v2, 0xbd1d265f, v86
	v_mul_f32_e32 v3, 0xbd1d265f, v88
	v_mul_f32_e32 v4, 0xbd1d265f, v82
	v_mul_f32_e32 v5, 0xbd1d265f, v84
	v_exp_f32_e32 v2, v2
	v_exp_f32_e32 v3, v3
	v_exp_f32_e32 v4, v4
	v_exp_f32_e32 v5, v5
	v_fma_f32 v2, v2, v246, v246
; #define LAS __attribute__((address_space(3)))
; __device__ __forceinline__ unsigned pk4_fp8(float a, float b, float c, float d) { int w = 0; w = __builtin_amdgcn_cvt_pk_fp8_f32(a, b, w, false); w = __builtin_amdgcn_cvt_pk_fp8_f32(c, d, w, true); return (unsigned)w; }
; __device__ __forceinline__ float swiglu1(float g, float l) {
;     g = fminf(g, 7.0f); l = fminf(fmaxf(l, -7.0f), 7.0f);
;     const float s = __builtin_amdgcn_rcpf(1.0f + __expf(-1.702f * g));
;     return g * s * (l + 1.0f);
; }
;     __device__ __forceinline__ void operator()(const f32x4 (&acc)[2][2][4][2], const Unit& u, int wr, int wc, int fr, int fq) const {
;     ...
;                 for (int bj = 0; bj < 2; ++bj) { const f32x4 v0 = acc[ai][bj][m][0] * scale + bv[bj][0], v1 = acc[ai][bj][m][1] * scale + bv[bj][1];
;                     *(LAS unsigned*)(wp + m * (32 * STG8_PITCH) + 64 * bj) = pk4_fp8(swiglu1(v0[0], v0[1]), swiglu1(v0[2], v0[3]), swiglu1(v1[0], v1[1]), swiglu1(v1[2], v1[3])); }
	v_fma_f32 v3, v3, v246, v246
	v_fma_f32 v4, v4, v246, v246
	v_fma_f32 v5, v5, v246, v246
	v_rcp_f32_e32 v2, v2
	v_rcp_f32_e32 v3, v3
	v_rcp_f32_e32 v4, v4
	v_rcp_f32_e32 v5, v5
	v_med3_f32 v87, v87, s47, v204
	v_med3_f32 v89, v89, s47, v204
	v_med3_f32 v83, v83, s47, v204
	v_med3_f32 v85, v85, s47, v204
	v_mul_f32_e32 v86, v86, v2
	v_mul_f32_e32 v88, v88, v3
	v_mul_f32_e32 v82, v82, v4
	v_mul_f32_e32 v84, v84, v5
	v_mul_f32_e32 v86, v86, v87
	v_mul_f32_e32 v88, v88, v89
	v_mul_f32_e32 v82, v82, v83
	v_mul_f32_e32 v84, v84, v85
	v_cvt_pk_fp8_f32 v27, v86, v88
	v_cvt_pk_fp8_f32 v27, v82, v84 op_sel:[0,0,1]
	v_min_f32_e32 v78, 0x43e00000, v78
	v_min_f32_e32 v80, 0x43e00000, v80
	v_min_f32_e32 v74, 0x43e00000, v74
	v_min_f32_e32 v76, 0x43e00000, v76
	v_mul_f32_e32 v2, 0xbd1d265f, v78
	v_mul_f32_e32 v3, 0xbd1d265f, v80
	v_mul_f32_e32 v4, 0xbd1d265f, v74
	v_mul_f32_e32 v5, 0xbd1d265f, v76
	v_exp_f32_e32 v2, v2
	v_exp_f32_e32 v3, v3
	v_exp_f32_e32 v4, v4
	v_exp_f32_e32 v5, v5
	v_fma_f32 v2, v2, v246, v246
	v_fma_f32 v3, v3, v246, v246
	v_fma_f32 v4, v4, v246, v246
	v_fma_f32 v5, v5, v246, v246
	v_rcp_f32_e32 v2, v2
	v_rcp_f32_e32 v3, v3
	v_rcp_f32_e32 v4, v4
	v_rcp_f32_e32 v5, v5
	v_med3_f32 v79, v79, s47, v204
	v_med3_f32 v81, v81, s47, v204
	v_med3_f32 v75, v75, s47, v204
	v_med3_f32 v77, v77, s47, v204
	v_mul_f32_e32 v78, v78, v2
	v_mul_f32_e32 v80, v80, v3
	v_mul_f32_e32 v74, v74, v4
	v_mul_f32_e32 v76, v76, v5
	v_mul_f32_e32 v78, v78, v79
	v_mul_f32_e32 v80, v80, v81
	v_mul_f32_e32 v74, v74, v75
	v_mul_f32_e32 v76, v76, v77
	v_cvt_pk_fp8_f32 v28, v78, v80
	v_cvt_pk_fp8_f32 v28, v74, v76 op_sel:[0,0,1]
	v_min_f32_e32 v70, 0x43e00000, v70
	v_min_f32_e32 v72, 0x43e00000, v72
	v_min_f32_e32 v66, 0x43e00000, v66
	v_min_f32_e32 v68, 0x43e00000, v68
	v_mul_f32_e32 v2, 0xbd1d265f, v70
	v_mul_f32_e32 v3, 0xbd1d265f, v72
	v_mul_f32_e32 v4, 0xbd1d265f, v66
	v_mul_f32_e32 v5, 0xbd1d265f, v68
	v_exp_f32_e32 v2, v2
	v_exp_f32_e32 v3, v3
	v_exp_f32_e32 v4, v4
	v_exp_f32_e32 v5, v5
	v_fma_f32 v2, v2, v246, v246
	v_fma_f32 v3, v3, v246, v246
	v_fma_f32 v4, v4, v246, v246
	v_fma_f32 v5, v5, v246, v246
	v_rcp_f32_e32 v2, v2
	v_rcp_f32_e32 v3, v3
	v_rcp_f32_e32 v4, v4
	v_rcp_f32_e32 v5, v5
	v_med3_f32 v71, v71, s47, v204
	v_med3_f32 v73, v73, s47, v204
	v_med3_f32 v67, v67, s47, v204
	v_med3_f32 v69, v69, s47, v204
	v_mul_f32_e32 v70, v70, v2
	v_mul_f32_e32 v72, v72, v3
	v_mul_f32_e32 v66, v66, v4
	v_mul_f32_e32 v68, v68, v5
	v_mul_f32_e32 v70, v70, v71
	v_mul_f32_e32 v72, v72, v73
	v_mul_f32_e32 v66, v66, v67
	v_mul_f32_e32 v68, v68, v69
	v_cvt_pk_fp8_f32 v29, v70, v72
	v_cvt_pk_fp8_f32 v29, v66, v68 op_sel:[0,0,1]
	v_min_f32_e32 v58, 0x43e00000, v58
	v_min_f32_e32 v60, 0x43e00000, v60
	v_min_f32_e32 v50, 0x43e00000, v50
	v_min_f32_e32 v52, 0x43e00000, v52
	v_mul_f32_e32 v2, 0xbd1d265f, v58
	v_mul_f32_e32 v3, 0xbd1d265f, v60
	v_mul_f32_e32 v4, 0xbd1d265f, v50
	v_mul_f32_e32 v5, 0xbd1d265f, v52
	v_exp_f32_e32 v2, v2
	v_exp_f32_e32 v3, v3
	v_exp_f32_e32 v4, v4
	v_exp_f32_e32 v5, v5
	v_fma_f32 v2, v2, v246, v246
	v_fma_f32 v3, v3, v246, v246
	v_fma_f32 v4, v4, v246, v246
	v_fma_f32 v5, v5, v246, v246
	v_rcp_f32_e32 v2, v2
	v_rcp_f32_e32 v3, v3
	v_rcp_f32_e32 v4, v4
	v_rcp_f32_e32 v5, v5
	v_med3_f32 v59, v59, s47, v204
	v_med3_f32 v61, v61, s47, v204
	v_med3_f32 v51, v51, s47, v204
	v_med3_f32 v53, v53, s47, v204
	v_mul_f32_e32 v58, v58, v2
	v_mul_f32_e32 v60, v60, v3
	v_mul_f32_e32 v50, v50, v4
	v_mul_f32_e32 v52, v52, v5
	v_mul_f32_e32 v58, v58, v59
	v_mul_f32_e32 v60, v60, v61
	v_mul_f32_e32 v50, v50, v51
	v_mul_f32_e32 v52, v52, v53
	v_cvt_pk_fp8_f32 v30, v58, v60
	v_cvt_pk_fp8_f32 v30, v50, v52 op_sel:[0,0,1]
	v_min_f32_e32 v62, 0x43e00000, v62
	v_min_f32_e32 v64, 0x43e00000, v64
	v_min_f32_e32 v54, 0x43e00000, v54
	v_min_f32_e32 v56, 0x43e00000, v56
	v_mul_f32_e32 v2, 0xbd1d265f, v62
	v_mul_f32_e32 v3, 0xbd1d265f, v64
	v_mul_f32_e32 v4, 0xbd1d265f, v54
	v_mul_f32_e32 v5, 0xbd1d265f, v56
	v_exp_f32_e32 v2, v2
	v_exp_f32_e32 v3, v3
	v_exp_f32_e32 v4, v4
	v_exp_f32_e32 v5, v5
	v_fma_f32 v2, v2, v246, v246
	v_fma_f32 v3, v3, v246, v246
	v_fma_f32 v4, v4, v246, v246
	v_fma_f32 v5, v5, v246, v246
	v_rcp_f32_e32 v2, v2
	v_rcp_f32_e32 v3, v3
	v_rcp_f32_e32 v4, v4
	v_rcp_f32_e32 v5, v5
	v_med3_f32 v63, v63, s47, v204
	v_med3_f32 v65, v65, s47, v204
	v_med3_f32 v55, v55, s47, v204
; #define LAS __attribute__((address_space(3)))
; __device__ __forceinline__ unsigned pk4_fp8(float a, float b, float c, float d) { int w = 0; w = __builtin_amdgcn_cvt_pk_fp8_f32(a, b, w, false); w = __builtin_amdgcn_cvt_pk_fp8_f32(c, d, w, true); return (unsigned)w; }
;     __device__ __forceinline__ void operator()(const f32x4 (&acc)[2][2][4][2], const Unit& u, int wr, int wc, int fr, int fq) const {
;     ...
;         for (int ai = 0; ai < 2; ++ai) {
; #pragma unroll
;             for (int m = 0; m < 4; ++m)
; #pragma unroll
;                 for (int bj = 0; bj < 2; ++bj) { const f32x4 v0 = acc[ai][bj][m][0] * scale + bv[bj][0], v1 = acc[ai][bj][m][1] * scale + bv[bj][1];
;                     *(LAS unsigned*)(wp + m * (32 * STG8_PITCH) + 64 * bj) = pk4_fp8(swiglu1(v0[0], v0[1]), swiglu1(v0[2], v0[3]), swiglu1(v1[0], v1[1]), swiglu1(v1[2], v1[3])); }
;             asm volatile("s_waitcnt lgkmcnt(0)" ::: "memory"); __builtin_amdgcn_s_barrier(); asm volatile("" ::: "memory");
; #pragma unroll
;             for (int k2 = 0; k2 < 2; ++k2) { const int m = ms + 2 * k2;
;                 *(u32x4*)(gp + (size_t)(ai * HALF + m * 16) * ldc) = *(const LAS u32x4*)(rp + m * (32 * STG8_PITCH)); }
;             asm volatile("s_waitcnt lgkmcnt(0)" ::: "memory"); __builtin_amdgcn_s_barrier(); asm volatile("" ::: "memory");
;         }
	v_med3_f32 v57, v57, s47, v204
	v_mul_f32_e32 v62, v62, v2
	v_mul_f32_e32 v64, v64, v3
	v_mul_f32_e32 v54, v54, v4
	v_mul_f32_e32 v56, v56, v5
	v_mul_f32_e32 v62, v62, v63
	v_mul_f32_e32 v64, v64, v65
	v_mul_f32_e32 v54, v54, v55
	v_mul_f32_e32 v56, v56, v57
	v_cvt_pk_fp8_f32 v31, v62, v64
	v_cvt_pk_fp8_f32 v31, v54, v56 op_sel:[0,0,1]
	v_min_f32_e32 v38, 0x43e00000, v38
	v_min_f32_e32 v40, 0x43e00000, v40
	v_min_f32_e32 v34, 0x43e00000, v34
	v_min_f32_e32 v36, 0x43e00000, v36
	v_mul_f32_e32 v2, 0xbd1d265f, v38
	v_mul_f32_e32 v3, 0xbd1d265f, v40
	v_mul_f32_e32 v4, 0xbd1d265f, v34
	v_mul_f32_e32 v5, 0xbd1d265f, v36
	v_exp_f32_e32 v2, v2
	v_exp_f32_e32 v3, v3
	v_exp_f32_e32 v4, v4
	v_exp_f32_e32 v5, v5
	v_fma_f32 v2, v2, v246, v246
	v_fma_f32 v3, v3, v246, v246
	v_fma_f32 v4, v4, v246, v246
	v_fma_f32 v5, v5, v246, v246
	v_rcp_f32_e32 v2, v2
	v_rcp_f32_e32 v3, v3
	v_rcp_f32_e32 v4, v4
	v_rcp_f32_e32 v5, v5
	v_med3_f32 v39, v39, s47, v204
	v_med3_f32 v41, v41, s47, v204
	v_med3_f32 v35, v35, s47, v204
	v_med3_f32 v37, v37, s47, v204
	v_mul_f32_e32 v38, v38, v2
	v_mul_f32_e32 v40, v40, v3
	v_mul_f32_e32 v34, v34, v4
	v_mul_f32_e32 v36, v36, v5
	v_mul_f32_e32 v38, v38, v39
	v_mul_f32_e32 v40, v40, v41
	v_mul_f32_e32 v34, v34, v35
	v_mul_f32_e32 v36, v36, v37
	v_cvt_pk_fp8_f32 v32, v38, v40
	v_cvt_pk_fp8_f32 v32, v34, v36 op_sel:[0,0,1]
	v_min_f32_e32 v46, 0x43e00000, v46
	v_min_f32_e32 v48, 0x43e00000, v48
	v_min_f32_e32 v42, 0x43e00000, v42
	v_min_f32_e32 v44, 0x43e00000, v44
	v_mul_f32_e32 v2, 0xbd1d265f, v46
	v_mul_f32_e32 v3, 0xbd1d265f, v48
	v_mul_f32_e32 v4, 0xbd1d265f, v42
	v_mul_f32_e32 v5, 0xbd1d265f, v44
	v_exp_f32_e32 v2, v2
	v_exp_f32_e32 v3, v3
	v_exp_f32_e32 v4, v4
	v_exp_f32_e32 v5, v5
	v_fma_f32 v2, v2, v246, v246
	v_fma_f32 v3, v3, v246, v246
	v_fma_f32 v4, v4, v246, v246
	v_fma_f32 v5, v5, v246, v246
	v_rcp_f32_e32 v2, v2
	v_rcp_f32_e32 v3, v3
	v_rcp_f32_e32 v4, v4
	v_rcp_f32_e32 v5, v5
	v_med3_f32 v47, v47, s47, v204
	v_med3_f32 v49, v49, s47, v204
	v_med3_f32 v43, v43, s47, v204
	v_med3_f32 v45, v45, s47, v204
	v_mul_f32_e32 v46, v46, v2
	v_mul_f32_e32 v48, v48, v3
	v_mul_f32_e32 v42, v42, v4
	v_mul_f32_e32 v44, v44, v5
	v_mul_f32_e32 v46, v46, v47
	v_mul_f32_e32 v48, v48, v49
	v_mul_f32_e32 v42, v42, v43
	v_mul_f32_e32 v44, v44, v45
	v_cvt_pk_fp8_f32 v33, v46, v48
	v_cvt_pk_fp8_f32 v33, v42, v44 op_sel:[0,0,1]
	v_add_u32_e32 v14, 0xfffe7000, v202
	v_add_u32_e32 v15, 0xfffe8000, v202
	v_add_u32_e32 v16, 0xfffe9400, v202
	v_add_u32_e32 v17, 0xfffea400, v202
	ds_write2_b32 v202, v6, v7 offset1:16
	ds_write2_b32 v22, v8, v9 offset0:128 offset1:144
	ds_write2_b32 v23, v10, v11 offset1:16
	ds_write2_b32 v24, v12, v13 offset0:128 offset1:144
	ds_write2_b32 v14, v26, v27 offset1:16
	ds_write2_b32 v15, v28, v29 offset0:128 offset1:144
	ds_write2_b32 v16, v30, v31 offset1:16
	ds_write2_b32 v17, v32, v33 offset0:128 offset1:144
	s_waitcnt lgkmcnt(0)
	s_barrier
	v_add_u32_e32 v14, 0xfffe7000, v203
	ds_read_b128 v[26:29], v203
	ds_read_b128 v[30:33], v203 offset:9216
	ds_read_b128 v[2:5], v14
	ds_read_b128 v[6:9], v14 offset:9216
	v_lshl_add_u64 v[20:21], v[18:19], 0, v[172:173]
	v_lshl_add_u64 v[18:19], v[18:19], 0, v[174:175]
	v_add_co_u32_e32 v10, vcc, s48, v20
	s_nop 1
	v_addc_co_u32_e32 v11, vcc, 0, v21, vcc
	v_add_co_u32_e32 v12, vcc, 0x40000, v18
	s_nop 1
	v_addc_co_u32_e32 v13, vcc, 0, v19, vcc
	s_waitcnt lgkmcnt(3)
	global_store_dwordx4 v[20:21], v[26:29], off
	s_waitcnt lgkmcnt(2)
	global_store_dwordx4 v[18:19], v[30:33], off
	s_waitcnt lgkmcnt(1)
	global_store_dwordx4 v[10:11], v[2:5], off
	s_waitcnt lgkmcnt(0)
	global_store_dwordx4 v[12:13], v[6:9], off
	s_barrier
	s_waitcnt vmcnt(4)
	v_mul_f32_e32 v208, v247, v208
	v_fma_f32 v209, v209, v247, v247
	v_mul_f32_e32 v210, v247, v210
	v_fma_f32 v211, v211, v247, v247
	v_mul_f32_e32 v212, v247, v212
	v_fma_f32 v213, v213, v247, v247
	v_mul_f32_e32 v214, v247, v214
	v_fma_f32 v215, v215, v247, v247
	v_mul_f32_e32 v216, v247, v216
	v_fma_f32 v217, v217, v247, v247
	v_mul_f32_e32 v218, v247, v218
	v_fma_f32 v219, v219, v247, v247
	v_mul_f32_e32 v220, v247, v220
	v_fma_f32 v221, v221, v247, v247
	v_mul_f32_e32 v222, v247, v222
	v_fma_f32 v223, v223, v247, v247
	s_cbranch_scc1 .LBB0_993
	s_andn2_b64 vcc, exec, s[6:7]
	s_cbranch_vccnz .LBB0_992
	s_barrier
	s_branch .LBB0_992
